# conversion loads use scalar base + lane offset (no 64-bit VALU address chain); attention prologue issues all ten K/V DMA requests before its first counted wait
# speedup vs baseline: 1.0135x; 1.0011x over previous
.LBB0_247:
	s_add_i32 s42, s64, s69
	s_mul_hi_i32 s71, s60, s42
	s_mul_i32 s70, s60, s42
	s_lshl_b64 s[70:71], s[70:71], 2
	s_add_u32 s42, s58, s70
	s_addc_u32 s70, s59, s71
	s_ashr_i32 s57, s56, 31
	s_lshl_b64 s[58:59], s[56:57], 2
	s_add_u32 s58, s42, s58
	s_addc_u32 s59, s70, s59
	s_lshl_b32 s42, s60, 2
	v_lshlrev_b32_e32 v166, 2, v132
	global_load_dwordx4 v[120:123], v166, s[58:59] nt
	s_add_u32 s58, s58, s42
	s_addc_u32 s59, s59, 0
	global_load_dwordx4 v[116:119], v166, s[58:59] nt
	s_add_u32 s58, s58, s42
	s_addc_u32 s59, s59, 0
	global_load_dwordx4 v[124:127], v166, s[58:59] nt
	s_add_u32 s58, s58, s42
	s_addc_u32 s59, s59, 0
	global_load_dwordx4 v[108:111], v166, s[58:59] nt
	s_add_u32 s58, s58, s42
	s_addc_u32 s59, s59, 0
	global_load_dwordx4 v[112:115], v166, s[58:59] nt
	s_add_u32 s58, s58, s42
	s_addc_u32 s59, s59, 0
	global_load_dwordx4 v[100:103], v166, s[58:59] nt
	s_add_u32 s58, s58, s42
	s_addc_u32 s59, s59, 0
	global_load_dwordx4 v[104:107], v166, s[58:59] nt
	s_add_u32 s58, s58, s42
	s_addc_u32 s59, s59, 0
	global_load_dwordx4 v[92:95], v166, s[58:59] nt
	s_add_u32 s58, s58, s42
	s_addc_u32 s59, s59, 0
	global_load_dwordx4 v[96:99], v166, s[58:59] nt
	s_add_u32 s58, s58, s42
	s_addc_u32 s59, s59, 0
	global_load_dwordx4 v[84:87], v166, s[58:59] nt
	s_add_u32 s58, s58, s42
	s_addc_u32 s59, s59, 0
	global_load_dwordx4 v[88:91], v166, s[58:59] nt
	s_add_u32 s58, s58, s42
	s_addc_u32 s59, s59, 0
	global_load_dwordx4 v[76:79], v166, s[58:59] nt
	s_add_u32 s58, s58, s42
	s_addc_u32 s59, s59, 0
	global_load_dwordx4 v[80:83], v166, s[58:59] nt
	s_add_u32 s58, s58, s42
	s_addc_u32 s59, s59, 0
	global_load_dwordx4 v[68:71], v166, s[58:59] nt
	s_add_u32 s58, s58, s42
	s_addc_u32 s59, s59, 0
	global_load_dwordx4 v[72:75], v166, s[58:59] nt
	s_add_u32 s58, s58, s42
	s_addc_u32 s59, s59, 0
	global_load_dwordx4 v[60:63], v166, s[58:59] nt
	s_add_u32 s58, s58, s42
	s_addc_u32 s59, s59, 0
	s_waitcnt vmcnt(24)
	v_mul_f32_e32 v162, 0x42000000, v64
	v_mul_f32_e32 v163, 0x42000000, v52
	v_mul_f32_e32 v164, 0x42000000, v56
	v_cvt_pk_fp8_f32 v158, v162, v163
	v_mul_f32_e32 v165, 0x42000000, v44
	v_cvt_pk_fp8_f32 v158, v164, v165 op_sel:[0,0,1]
	v_mul_f32_e32 v162, 0x42000000, v48
	v_mul_f32_e32 v163, 0x42000000, v36
	v_mul_f32_e32 v164, 0x42000000, v40
	v_cvt_pk_fp8_f32 v159, v162, v163
	v_mul_f32_e32 v165, 0x42000000, v28
	v_cvt_pk_fp8_f32 v159, v164, v165 op_sel:[0,0,1]
	v_mul_f32_e32 v162, 0x42000000, v32
	v_mul_f32_e32 v163, 0x42000000, v20
	v_mul_f32_e32 v164, 0x42000000, v24
	v_cvt_pk_fp8_f32 v160, v162, v163
	v_mul_f32_e32 v165, 0x42000000, v12
	v_cvt_pk_fp8_f32 v160, v164, v165 op_sel:[0,0,1]
	v_mul_f32_e32 v162, 0x42000000, v16
	v_mul_f32_e32 v163, 0x42000000, v4
	v_mul_f32_e32 v164, 0x42000000, v8
	v_cvt_pk_fp8_f32 v161, v162, v163
	v_mul_f32_e32 v165, 0x42000000, v128
	v_cvt_pk_fp8_f32 v161, v164, v165 op_sel:[0,0,1]
	ds_write_b128 v156, v[158:161]
	v_mul_f32_e32 v162, 0x42000000, v65
	v_mul_f32_e32 v163, 0x42000000, v53
	v_mul_f32_e32 v164, 0x42000000, v57
	v_cvt_pk_fp8_f32 v168, v162, v163
	v_mul_f32_e32 v165, 0x42000000, v45
	v_cvt_pk_fp8_f32 v168, v164, v165 op_sel:[0,0,1]
	v_mul_f32_e32 v162, 0x42000000, v49
	v_mul_f32_e32 v163, 0x42000000, v37
	v_mul_f32_e32 v164, 0x42000000, v41
	v_cvt_pk_fp8_f32 v169, v162, v163
	v_mul_f32_e32 v165, 0x42000000, v29
	v_cvt_pk_fp8_f32 v169, v164, v165 op_sel:[0,0,1]
	v_mul_f32_e32 v162, 0x42000000, v33
	v_mul_f32_e32 v163, 0x42000000, v21
	v_mul_f32_e32 v164, 0x42000000, v25
	v_cvt_pk_fp8_f32 v170, v162, v163
	v_mul_f32_e32 v165, 0x42000000, v13
	v_cvt_pk_fp8_f32 v170, v164, v165 op_sel:[0,0,1]
	v_mul_f32_e32 v162, 0x42000000, v17
	v_mul_f32_e32 v163, 0x42000000, v5
	v_mul_f32_e32 v164, 0x42000000, v9
	v_cvt_pk_fp8_f32 v171, v162, v163
	v_mul_f32_e32 v165, 0x42000000, v129
	v_cvt_pk_fp8_f32 v171, v164, v165 op_sel:[0,0,1]
	ds_write_b128 v156, v[168:171] offset:256
	v_mul_f32_e32 v162, 0x42000000, v66
	v_mul_f32_e32 v163, 0x42000000, v54
	v_mul_f32_e32 v164, 0x42000000, v58
	v_cvt_pk_fp8_f32 v158, v162, v163
	v_mul_f32_e32 v165, 0x42000000, v46
	v_cvt_pk_fp8_f32 v158, v164, v165 op_sel:[0,0,1]
	v_mul_f32_e32 v162, 0x42000000, v50
	v_mul_f32_e32 v163, 0x42000000, v38
	v_mul_f32_e32 v164, 0x42000000, v42
	v_cvt_pk_fp8_f32 v159, v162, v163
	v_mul_f32_e32 v165, 0x42000000, v30
	v_cvt_pk_fp8_f32 v159, v164, v165 op_sel:[0,0,1]
	v_mul_f32_e32 v162, 0x42000000, v34
	v_mul_f32_e32 v163, 0x42000000, v22
	v_mul_f32_e32 v164, 0x42000000, v26
	v_cvt_pk_fp8_f32 v160, v162, v163
	v_mul_f32_e32 v165, 0x42000000, v14
	v_cvt_pk_fp8_f32 v160, v164, v165 op_sel:[0,0,1]
	v_mul_f32_e32 v162, 0x42000000, v18
	v_mul_f32_e32 v163, 0x42000000, v6
	v_mul_f32_e32 v164, 0x42000000, v10
	v_cvt_pk_fp8_f32 v161, v162, v163
	v_mul_f32_e32 v165, 0x42000000, v130
	v_cvt_pk_fp8_f32 v161, v164, v165 op_sel:[0,0,1]
	ds_write_b128 v156, v[158:161] offset:512
	v_mul_f32_e32 v162, 0x42000000, v67
	v_mul_f32_e32 v163, 0x42000000, v55
	v_mul_f32_e32 v164, 0x42000000, v59
	v_cvt_pk_fp8_f32 v168, v162, v163
	v_mul_f32_e32 v165, 0x42000000, v47
	v_cvt_pk_fp8_f32 v168, v164, v165 op_sel:[0,0,1]
	v_mul_f32_e32 v162, 0x42000000, v51
	v_mul_f32_e32 v163, 0x42000000, v39
	v_mul_f32_e32 v164, 0x42000000, v43
	v_cvt_pk_fp8_f32 v169, v162, v163
	v_mul_f32_e32 v165, 0x42000000, v31
	v_cvt_pk_fp8_f32 v169, v164, v165 op_sel:[0,0,1]
	v_mul_f32_e32 v162, 0x42000000, v35
	v_mul_f32_e32 v163, 0x42000000, v23
	v_mul_f32_e32 v164, 0x42000000, v27
	v_cvt_pk_fp8_f32 v170, v162, v163
	v_mul_f32_e32 v165, 0x42000000, v15
	v_cvt_pk_fp8_f32 v170, v164, v165 op_sel:[0,0,1]
	v_mul_f32_e32 v162, 0x42000000, v19
	v_mul_f32_e32 v163, 0x42000000, v7
	v_mul_f32_e32 v164, 0x42000000, v11
	v_cvt_pk_fp8_f32 v171, v162, v163
	v_mul_f32_e32 v165, 0x42000000, v131
	v_cvt_pk_fp8_f32 v171, v164, v165 op_sel:[0,0,1]
	ds_write_b128 v156, v[168:171] offset:768
	global_load_dwordx4 v[64:67], v166, s[58:59] nt
	s_add_u32 s58, s58, s42
	s_addc_u32 s59, s59, 0
	global_load_dwordx4 v[52:55], v166, s[58:59] nt
	s_add_u32 s58, s58, s42
	s_addc_u32 s59, s59, 0
	global_load_dwordx4 v[56:59], v166, s[58:59] nt
	s_add_u32 s58, s58, s42
	s_addc_u32 s59, s59, 0
	global_load_dwordx4 v[44:47], v166, s[58:59] nt
	s_add_u32 s58, s58, s42
	s_addc_u32 s59, s59, 0
	global_load_dwordx4 v[48:51], v166, s[58:59] nt
	s_add_u32 s58, s58, s42
	s_addc_u32 s59, s59, 0
	global_load_dwordx4 v[36:39], v166, s[58:59] nt
	s_add_u32 s58, s58, s42
	s_addc_u32 s59, s59, 0
	global_load_dwordx4 v[40:43], v166, s[58:59] nt
	s_add_u32 s58, s58, s42
	s_addc_u32 s59, s59, 0
	global_load_dwordx4 v[28:31], v166, s[58:59] nt
	s_add_u32 s58, s58, s42
	s_addc_u32 s59, s59, 0
	global_load_dwordx4 v[32:35], v166, s[58:59] nt
	s_add_u32 s58, s58, s42
	s_addc_u32 s59, s59, 0
	global_load_dwordx4 v[20:23], v166, s[58:59] nt
	s_add_u32 s58, s58, s42
	s_addc_u32 s59, s59, 0
	global_load_dwordx4 v[24:27], v166, s[58:59] nt
	s_add_u32 s58, s58, s42
	s_addc_u32 s59, s59, 0
	global_load_dwordx4 v[12:15], v166, s[58:59] nt
	s_add_u32 s58, s58, s42
	s_addc_u32 s59, s59, 0
	global_load_dwordx4 v[16:19], v166, s[58:59] nt
	s_add_u32 s58, s58, s42
	s_addc_u32 s59, s59, 0
	global_load_dwordx4 v[4:7], v166, s[58:59] nt
	s_add_u32 s58, s58, s42
	s_addc_u32 s59, s59, 0
	global_load_dwordx4 v[8:11], v166, s[58:59] nt
	s_add_u32 s58, s58, s42
	s_addc_u32 s59, s59, 0
	global_load_dwordx4 v[128:131], v166, s[58:59] nt
	s_add_u32 s58, s58, s42
	s_addc_u32 s59, s59, 0
	v_mov_b32_e32 v154, s61
	s_branch .Lcv_join

.LBB0_334:
	s_and_b64 vcc, exec, s[60:61]
	s_cbranch_vccz .LBB0_242
	v_readlane_b32 s10, v254, 20
	s_add_u32 s10, s10, s56
	v_readlane_b32 s11, v254, 19
	s_addc_u32 s11, s11, s57
	s_add_u32 s14, s10, s58
	s_addc_u32 s15, s11, s59
	s_lshl_b64 s[90:91], s[54:55], 1
	s_add_u32 s10, s73, s90
	v_readfirstlane_b32 s11, v235
	s_addc_u32 s44, s75, s91
	s_lshr_b32 s42, s11, 6
	s_lshl_b32 s53, s42, 5
	s_mul_i32 s54, s42, 0xc000
	s_mul_hi_u32 s55, s53, 0x600
	s_lshl_b64 vcc, s[54:55], 1
	s_add_u32 s62, s10, vcc_lo
	s_addc_u32 s63, s44, vcc_hi
	s_lshl_b32 s10, s42, 4
	v_add_u32_e32 v165, s10, v208
	v_and_or_b32 v0, s10, 48, v201
	s_lshr_b32 s10, s11, 3
	s_and_b32 s10, s10, 0x1fffffe0
	s_lshl_b32 s44, s42, 10
	v_mov_b32_e32 v2, s10
	s_movk_i32 s10, 0x180
	s_cmp_lg_u32 0, -1
	v_mad_u32_u24 v0, v0, s10, v2
	s_cselect_b32 s10, 0, 0
	s_add_i32 s70, s44, s10
	v_or_b32_e32 v0, v0, v209
	s_add_i32 s10, s70, 0xc000
	s_mov_b32 m0, s70
	s_nop 0
	global_load_lds_dwordx4 v165, s[88:89]
	v_lshlrev_b32_e32 v164, 1, v0
	s_mov_b32 m0, s10
	s_nop 0
	global_load_lds_dwordx4 v164, s[14:15]
	s_add_u32 s54, s88, 0xc000
	s_addc_u32 s55, s89, 0
	s_add_i32 s71, s70, 0x2000
	s_mov_b32 m0, s71
	s_nop 0
	global_load_lds_dwordx4 v165, s[54:55]
	global_load_dwordx4 v[140:143], v217, s[62:63]
	global_load_dwordx4 v[128:131], v217, s[62:63] offset:32
	global_load_dwordx4 v[136:139], v217, s[62:63] offset:64
	global_load_dwordx4 v[132:135], v217, s[62:63] offset:96
	s_add_u32 s64, s88, 0x18000
	s_addc_u32 s65, s89, 0
	s_add_i32 s76, s70, 0x4000
	s_add_u32 s62, s88, 0x24000
	s_mov_b32 m0, s76
	s_nop 0
	global_load_lds_dwordx4 v165, s[64:65]
	s_addc_u32 s63, s89, 0
	s_add_i32 s77, s70, 0x6000
	s_mov_b32 m0, s77
	s_nop 0
	global_load_lds_dwordx4 v165, s[62:63]
	s_add_u32 s62, s14, 0xc000
	s_addc_u32 s63, s15, 0
	s_add_i32 s78, s70, 0xe000
	s_mov_b32 m0, s78
	s_nop 0
	global_load_lds_dwordx4 v164, s[62:63]
	s_add_u32 s62, s88, 0x30000
	s_addc_u32 s63, s89, 0
	s_add_i32 s79, s70, 0x8000
	s_mov_b32 m0, s79
	s_nop 0
	global_load_lds_dwordx4 v165, s[62:63]
	s_add_u32 s62, s88, 0x3c000
	s_addc_u32 s63, s89, 0
	s_add_i32 s85, s70, 0xa000
	s_mov_b32 m0, s85
	s_nop 0
	global_load_lds_dwordx4 v165, s[62:63]
	s_add_u32 s62, s14, 0x18000
	s_addc_u32 s63, s15, 0
	s_add_i32 s92, s70, 0x10000
	s_mov_b32 m0, s92
	s_nop 0
	global_load_lds_dwordx4 v164, s[62:63]
	s_add_u32 s62, s14, 0x24000
	s_addc_u32 s63, s15, 0
	s_add_i32 s93, s70, 0x12000
	s_mov_b32 m0, s93
	s_nop 0
	global_load_lds_dwordx4 v164, s[62:63]
	s_waitcnt vmcnt(7) lgkmcnt(0)
	s_barrier
	s_waitcnt vmcnt(22)
	ds_read_b128 v[36:39], v210
	s_waitcnt vmcnt(21)
	ds_read_b128 v[40:43], v210 offset:512
	s_mov_b32 s53, s52
	s_mov_b32 s54, s52
	s_mov_b32 s55, s52
	s_mov_b32 s56, s52
	s_mov_b32 s57, s52
	s_mov_b32 s58, s52
	s_mov_b32 s59, s52
	s_mov_b32 s60, s52
	s_mov_b32 s61, s52
	s_mov_b32 s62, s52
	s_mov_b32 s63, s52
	s_mov_b32 s64, s52
	s_mov_b32 s65, s52
	s_mov_b32 s66, s52
	s_mov_b32 s67, s52
	s_waitcnt vmcnt(13)
	v_mov_b64_e32 v[4:5], s[52:53]
	v_mov_b64_e32 v[6:7], s[54:55]
	v_mov_b64_e32 v[8:9], s[56:57]
	v_mov_b64_e32 v[10:11], s[58:59]
	v_mov_b64_e32 v[12:13], s[60:61]
	v_mov_b64_e32 v[14:15], s[62:63]
	v_mov_b64_e32 v[16:17], s[64:65]
	v_mov_b64_e32 v[18:19], s[66:67]
	v_mov_b32_e32 v148, 0
	v_mov_b32_e32 v2, 0
	v_mov_b32_e32 v72, 0
	s_mov_b32 s53, -5
	s_waitcnt lgkmcnt(1)
	v_mfma_f32_32x32x16_bf16 v[20:35], v[36:39], v[140:143], v[4:19]
	s_mov_b64 s[54:55], 0
	v_mov_b32_e32 v73, 0
	v_mov_b32_e32 v149, v148
	v_mov_b32_e32 v150, v148
	v_mov_b32_e32 v151, v148
	s_waitcnt lgkmcnt(0)
	v_mfma_f32_32x32x16_bf16 v[4:19], v[40:43], v[140:143], v[4:19]
	ds_read_b128 v[36:39], v210 offset:2048
	ds_read_b128 v[40:43], v210 offset:2560
	s_waitcnt lgkmcnt(1)
	v_mfma_f32_32x32x16_bf16 v[20:35], v[36:39], v[128:131], v[20:35]
	s_waitcnt lgkmcnt(0)
	v_mfma_f32_32x32x16_bf16 v[4:19], v[40:43], v[128:131], v[4:19]
	ds_read_b128 v[36:39], v210 offset:4096
	ds_read_b128 v[40:43], v210 offset:4608
	s_waitcnt lgkmcnt(1)
	v_mfma_f32_32x32x16_bf16 v[20:35], v[36:39], v[136:139], v[20:35]
	s_waitcnt lgkmcnt(0)
	v_mfma_f32_32x32x16_bf16 v[4:19], v[40:43], v[136:139], v[4:19]
	ds_read_b128 v[36:39], v210 offset:6144
	ds_read_b128 v[40:43], v210 offset:6656
	s_waitcnt lgkmcnt(1)
	v_mfma_f32_32x32x16_bf16 v[20:35], v[36:39], v[132:135], v[20:35]
	s_waitcnt lgkmcnt(0)
	v_mfma_f32_32x32x16_bf16 v[4:19], v[40:43], v[132:135], v[4:19]
	s_nop 15
	s_nop 7
	s_waitcnt vmcnt(4) lgkmcnt(0)
	s_barrier
	ds_read_b128 v[68:71], v210 offset:8192
	ds_read_b128 v[160:163], v210 offset:8704
	ds_read_b128 v[156:159], v210 offset:10240
	ds_read_b128 v[112:115], v210 offset:10752
	ds_read_b128 v[152:155], v210 offset:12288
	ds_read_b128 v[104:107], v210 offset:12800
	ds_read_b128 v[108:111], v210 offset:14336
	ds_read_b128 v[100:103], v210 offset:14848
	s_nop 1
	v_exp_f32_e32 v52, v20
	v_exp_f32_e32 v53, v21
	v_exp_f32_e32 v54, v22
	v_exp_f32_e32 v55, v23
	v_exp_f32_e32 v56, v24
	v_exp_f32_e32 v57, v25
	v_exp_f32_e32 v58, v26
	v_exp_f32_e32 v59, v27
	v_exp_f32_e32 v60, v28
	v_exp_f32_e32 v61, v29
	v_exp_f32_e32 v62, v30
	v_exp_f32_e32 v63, v31
	v_exp_f32_e32 v64, v32
	v_exp_f32_e32 v65, v33
	v_exp_f32_e32 v66, v34
	v_exp_f32_e32 v67, v35
	v_exp_f32_e32 v36, v4
	v_exp_f32_e32 v37, v5
	v_exp_f32_e32 v38, v6
	v_exp_f32_e32 v39, v7
	v_exp_f32_e32 v40, v8
	v_exp_f32_e32 v41, v9
	v_exp_f32_e32 v42, v10
	v_exp_f32_e32 v43, v11
	v_mov_b32_e32 v44, v12
	v_mov_b32_e32 v45, v13
	v_mov_b32_e32 v46, v14
	v_mov_b32_e32 v47, v15
	v_mov_b32_e32 v48, v16
	v_mov_b32_e32 v49, v17
	v_mov_b32_e32 v50, v18
	v_mov_b32_e32 v51, v19
	s_waitcnt vmcnt(4) lgkmcnt(0)
	s_barrier
	v_mov_b32_e32 v4, 0
	v_mov_b32_e32 v5, v2
	v_mov_b32_e32 v6, v2
	v_mov_b32_e32 v7, v2
	v_mov_b32_e32 v8, v2
	v_mov_b32_e32 v9, v2
	v_mov_b32_e32 v10, v2
	v_mov_b32_e32 v11, v2
	v_mov_b32_e32 v12, v2
	v_mov_b32_e32 v13, v2
	v_mov_b32_e32 v14, v2
	v_mov_b32_e32 v15, v2
	v_mov_b32_e32 v16, v2
	v_mov_b32_e32 v17, v2
	v_mov_b32_e32 v18, v2
	v_mov_b32_e32 v19, v2
	v_mov_b32_e32 v20, 0
	v_mov_b32_e32 v21, v2
	v_mov_b32_e32 v22, v2
	v_mov_b32_e32 v23, v2
	v_mov_b32_e32 v24, v2
	v_mov_b32_e32 v25, v2
	v_mov_b32_e32 v26, v2
	v_mov_b32_e32 v27, v2
	v_mov_b32_e32 v28, v2
	v_mov_b32_e32 v29, v2
	v_mov_b32_e32 v30, v2
	v_mov_b32_e32 v31, v2
	v_mov_b32_e32 v32, v2
	v_mov_b32_e32 v33, v2
	v_mov_b32_e32 v34, v2
	v_mov_b32_e32 v35, v2
